# SSD pass B gated RMS norm: 160 serial ds_bpermute butterfly hops replaced by DPP moves / permlane16_swap (bit-identical sums), on top of v66
# speedup vs baseline: 1.0123x; 1.0057x over previous
.LBB0_829:
	s_mul_i32 s0, s65, 0x2c00
	s_mul_hi_u32 s1, s64, 0x2c00
	s_add_i32 s1, s1, s0
	s_mul_i32 s0, s64, 0x2c00
	s_add_u32 s0, s44, s0
	v_lshlrev_b32_e32 v66, 6, v148
	s_addc_u32 s1, s45, s1
	v_ashrrev_i32_e32 v67, 31, v66
	v_lshl_add_u64 v[68:69], v[66:67], 1, s[0:1]
	v_lshlrev_b32_e32 v146, 1, v195
	v_lshl_add_u64 v[76:77], v[68:69], 0, v[146:147]
	v_mul_u32_u24_e32 v70, 0x2c00, v209
	v_mov_b32_e32 v71, v147
	v_lshl_add_u64 v[70:71], v[76:77], 0, v[70:71]
	v_mul_u32_u24_e32 v68, 0xb000, v194
	v_mov_b32_e32 v69, v147
	v_add_co_u32_e32 v72, vcc, s78, v70
	v_lshl_add_u64 v[68:69], v[76:77], 0, v[68:69]
	s_nop 0
	v_addc_co_u32_e32 v73, vcc, 0, v71, vcc
	v_mad_u32_u24 v78, v209, s79, v1
	v_mov_b32_e32 v79, v147
	v_lshl_add_u64 v[74:75], v[70:71], 0, s[58:59]
	v_lshl_add_u64 v[78:79], v[76:77], 0, v[78:79]
	global_load_ushort v140, v[68:69], off
	s_nop 0
	global_load_ushort v68, v[68:69], off offset:64
	s_nop 0
	global_load_ushort v135, v[70:71], off
	global_load_ushort v69, v[70:71], off offset:64
	s_nop 0
	global_load_ushort v72, v[72:73], off offset:3072
	s_nop 0
	global_load_ushort v73, v[78:79], off
	global_load_ushort v71, v[78:79], off offset:64
	global_load_ushort v70, v[74:75], off offset:64
	v_mad_u32_u24 v74, v209, s79, v152
	v_mov_b32_e32 v75, v147
	v_mad_u32_u24 v78, v209, s79, v153
	v_mov_b32_e32 v79, v147
	s_waitcnt vmcnt(8)
	v_mad_u32_u24 v82, v209, s79, v155
	v_mov_b32_e32 v83, v147
	v_lshl_add_u64 v[74:75], v[76:77], 0, v[74:75]
	v_lshl_add_u64 v[78:79], v[76:77], 0, v[78:79]
	v_mad_u32_u24 v80, v209, s79, v154
	v_mov_b32_e32 v81, v147
	v_lshl_add_u64 v[82:83], v[76:77], 0, v[82:83]
	v_lshl_add_u64 v[80:81], v[76:77], 0, v[80:81]
	global_load_ushort v134, v[74:75], off
	global_load_ushort v133, v[74:75], off offset:64
	global_load_ushort v132, v[78:79], off
	global_load_ushort v131, v[78:79], off offset:64
	global_load_ushort v130, v[80:81], off
	global_load_ushort v129, v[80:81], off offset:64
	global_load_ushort v128, v[82:83], off
	global_load_ushort v74, v[82:83], off offset:64
	v_mad_u32_u24 v78, v209, s79, v156
	v_mov_b32_e32 v79, v147
	v_mad_u32_u24 v82, v209, s79, v158
	v_mov_b32_e32 v83, v147
	v_mad_u32_u24 v84, v209, s79, v159
	v_mov_b32_e32 v85, v147
	v_lshl_add_u64 v[78:79], v[76:77], 0, v[78:79]
	v_mad_u32_u24 v80, v209, s79, v157
	v_mov_b32_e32 v81, v147
	v_lshl_add_u64 v[82:83], v[76:77], 0, v[82:83]
	v_lshl_add_u64 v[84:85], v[76:77], 0, v[84:85]
	v_lshl_add_u64 v[80:81], v[76:77], 0, v[80:81]
	global_load_ushort v127, v[78:79], off
	global_load_ushort v126, v[78:79], off offset:64
	global_load_ushort v125, v[80:81], off
	global_load_ushort v124, v[80:81], off offset:64
	global_load_ushort v123, v[82:83], off
	global_load_ushort v122, v[82:83], off offset:64
	global_load_ushort v121, v[84:85], off
	global_load_ushort v75, v[84:85], off offset:64
	v_mad_u32_u24 v78, v209, s79, v160
	v_mov_b32_e32 v79, v147
	v_mad_u32_u24 v82, v209, s79, v162
	v_mov_b32_e32 v83, v147
	v_mad_u32_u24 v84, v209, s79, v163
	v_mov_b32_e32 v85, v147
	v_lshl_add_u64 v[78:79], v[76:77], 0, v[78:79]
	v_mad_u32_u24 v80, v209, s79, v161
	v_mov_b32_e32 v81, v147
	v_lshl_add_u64 v[82:83], v[76:77], 0, v[82:83]
	v_lshl_add_u64 v[84:85], v[76:77], 0, v[84:85]
	v_lshl_add_u64 v[80:81], v[76:77], 0, v[80:81]
	global_load_ushort v120, v[78:79], off
	global_load_ushort v119, v[78:79], off offset:64
	global_load_ushort v118, v[80:81], off
	global_load_ushort v117, v[80:81], off offset:64
	global_load_ushort v116, v[82:83], off
	global_load_ushort v115, v[82:83], off offset:64
	global_load_ushort v114, v[84:85], off
	global_load_ushort v113, v[84:85], off offset:64
	v_mad_u32_u24 v78, v209, s79, v164
	v_mov_b32_e32 v79, v147
	v_mad_u32_u24 v82, v209, s79, v166
	v_mov_b32_e32 v83, v147
	v_mad_u32_u24 v84, v209, s79, v167
	v_mov_b32_e32 v85, v147
	v_lshl_add_u64 v[78:79], v[76:77], 0, v[78:79]
	v_mad_u32_u24 v80, v209, s79, v165
	v_mov_b32_e32 v81, v147
	v_lshl_add_u64 v[82:83], v[76:77], 0, v[82:83]
	v_lshl_add_u64 v[84:85], v[76:77], 0, v[84:85]
	v_lshl_add_u64 v[80:81], v[76:77], 0, v[80:81]
	global_load_ushort v112, v[78:79], off
	global_load_ushort v111, v[78:79], off offset:64
	global_load_ushort v110, v[80:81], off
	global_load_ushort v109, v[80:81], off offset:64
	global_load_ushort v108, v[82:83], off
	global_load_ushort v107, v[82:83], off offset:64
	global_load_ushort v106, v[84:85], off
	global_load_ushort v105, v[84:85], off offset:64
	v_mad_u32_u24 v78, v209, s79, v168
	v_mov_b32_e32 v79, v147
	v_mad_u32_u24 v82, v209, s79, v170
	v_mov_b32_e32 v83, v147
	v_mad_u32_u24 v84, v209, s79, v171
	v_mov_b32_e32 v85, v147
	v_lshl_add_u64 v[78:79], v[76:77], 0, v[78:79]
	v_mad_u32_u24 v80, v209, s79, v169
	v_mov_b32_e32 v81, v147
	v_lshl_add_u64 v[82:83], v[76:77], 0, v[82:83]
	v_lshl_add_u64 v[84:85], v[76:77], 0, v[84:85]
	v_lshl_add_u64 v[80:81], v[76:77], 0, v[80:81]
	global_load_ushort v104, v[78:79], off
	global_load_ushort v103, v[78:79], off offset:64
	global_load_ushort v102, v[80:81], off
	global_load_ushort v101, v[80:81], off offset:64
	global_load_ushort v100, v[82:83], off
	global_load_ushort v99, v[82:83], off offset:64
	global_load_ushort v98, v[84:85], off
	s_nop 0
	global_load_ushort v85, v[84:85], off offset:64
	v_mad_u32_u24 v78, v209, s79, v172
	v_mov_b32_e32 v79, v147
	v_mad_u32_u24 v82, v209, s79, v174
	v_mov_b32_e32 v83, v147
	v_lshl_add_u64 v[78:79], v[76:77], 0, v[78:79]
	v_mad_u32_u24 v80, v209, s79, v173
	v_mov_b32_e32 v81, v147
	v_lshl_add_u64 v[82:83], v[76:77], 0, v[82:83]
	v_mad_u32_u24 v86, v209, s79, v175
	v_mov_b32_e32 v87, v147
	v_lshl_add_u64 v[80:81], v[76:77], 0, v[80:81]
	v_lshl_add_u64 v[86:87], v[76:77], 0, v[86:87]
	global_load_ushort v97, v[78:79], off
	global_load_ushort v96, v[78:79], off offset:64
	global_load_ushort v95, v[80:81], off
	global_load_ushort v94, v[80:81], off offset:64
	global_load_ushort v93, v[82:83], off
	global_load_ushort v92, v[82:83], off offset:64
	global_load_ushort v91, v[86:87], off
	global_load_ushort v90, v[86:87], off offset:64
	v_mad_u32_u24 v78, v209, s79, v176
	v_mov_b32_e32 v79, v147
	v_mad_u32_u24 v82, v209, s79, v178
	v_mov_b32_e32 v83, v147
	v_lshl_add_u64 v[78:79], v[76:77], 0, v[78:79]
	v_mad_u32_u24 v80, v209, s79, v177
	v_mov_b32_e32 v81, v147
	v_lshl_add_u64 v[136:137], v[76:77], 0, v[82:83]
	v_mad_u32_u24 v82, v209, s79, v179
	v_lshl_add_u64 v[80:81], v[76:77], 0, v[80:81]
	v_lshl_add_u64 v[138:139], v[76:77], 0, v[82:83]
	global_load_ushort v89, v[78:79], off
	global_load_ushort v88, v[78:79], off offset:64
	global_load_ushort v87, v[80:81], off
	global_load_ushort v86, v[80:81], off offset:64
	global_load_ushort v82, v[136:137], off
	s_nop 0
	global_load_ushort v79, v[136:137], off offset:64
	global_load_ushort v77, v[138:139], off
	global_load_ushort v76, v[138:139], off offset:64
	v_and_b32_e32 v80, 64, v212
	v_add_u32_e32 v83, 64, v80
	s_waitcnt vmcnt(62)
	v_lshlrev_b32_e32 v80, 16, v140
	v_mul_f32_e32 v81, 0xbfb8aa3b, v80
	v_lshlrev_b32_e32 v84, 16, v68
	v_exp_f32_e32 v81, v81
	v_mul_f32_e32 v68, 0xbfb8aa3b, v84
	v_exp_f32_e32 v68, v68
	v_mul_f32_e32 v2, v2, v80
	v_add_f32_e32 v81, 1.0, v81
	v_rcp_f32_e32 v81, v81
	v_add_f32_e32 v68, 1.0, v68
	v_rcp_f32_e32 v136, v68
	v_xor_b32_e32 v78, 16, v212
	v_mul_f32_e32 v68, v2, v81
	v_mul_f32_e32 v2, v50, v84
	v_cmp_lt_i32_e32 vcc, v78, v83
	v_mul_f32_e32 v50, v2, v136
	v_mul_f32_e32 v80, v50, v50
	v_cndmask_b32_e32 v78, v212, v78, vcc
	v_lshlrev_b32_e32 v78, 2, v78
	v_fmac_f32_e32 v80, v68, v68
	v_mov_b32_e32 v81, v80
	s_nop 1
	v_permlane16_swap_b32_e32 v81, v80
	v_xor_b32_e32 v2, 8, v212
	v_cmp_lt_i32_e32 vcc, v2, v83
	v_add_f32_e32 v81, v80, v81
	v_cndmask_b32_e32 v2, v212, v2, vcc
	v_lshlrev_b32_e32 v2, 2, v2
	s_nop 1
	v_mov_b32_dpp v84, v81 row_ror:8 row_mask:0xf bank_mask:0xf
	v_xor_b32_e32 v80, 4, v212
	v_cmp_lt_i32_e32 vcc, v80, v83
	v_add_f32_e32 v84, v81, v84
	v_cndmask_b32_e32 v80, v212, v80, vcc
	v_lshlrev_b32_e32 v80, 2, v80
	s_nop 1
	v_mov_b32_dpp v136, v84 row_shr:4 row_mask:0xf bank_mask:0xa
	v_mov_b32_dpp v136, v84 row_shl:4 row_mask:0xf bank_mask:0x5
	v_xor_b32_e32 v81, 2, v212
	v_cmp_lt_i32_e32 vcc, v81, v83
	v_add_f32_e32 v136, v84, v136
	v_cndmask_b32_e32 v81, v212, v81, vcc
	v_lshlrev_b32_e32 v81, 2, v81
	s_nop 1
	v_mov_b32_dpp v137, v136 quad_perm:[2,3,0,1] row_mask:0xf bank_mask:0xf
	v_xor_b32_e32 v84, 1, v212
	v_cmp_lt_i32_e32 vcc, v84, v83
	v_add_f32_e32 v136, v136, v137
	v_cndmask_b32_e32 v83, v212, v84, vcc
	v_lshlrev_b32_e32 v84, 2, v83
	s_nop 1
	v_mov_b32_dpp v137, v136 quad_perm:[1,0,3,2] row_mask:0xf bank_mask:0xf
	v_lshl_add_u32 v83, v213, 2, s80
	v_cmp_eq_u32_e32 vcc, 0, v195
	v_add_u32_e32 v83, v83, v214
	s_and_saveexec_b64 s[6:7], vcc
	s_cbranch_execz .LBB0_831
	v_add_f32_e32 v136, v136, v137
	ds_write_b32 v83, v136
.LBB0_831:
	s_or_b64 exec, exec, s[6:7]
	s_waitcnt vmcnt(61)
	v_lshlrev_b32_e32 v135, 16, v135
	v_mul_f32_e32 v136, 0xbfb8aa3b, v135
	s_waitcnt vmcnt(60)
	v_lshlrev_b32_e32 v137, 16, v69
	v_exp_f32_e32 v136, v136
	v_mul_f32_e32 v69, 0xbfb8aa3b, v137
	v_exp_f32_e32 v69, v69
	v_mul_f32_e32 v3, v3, v135
	v_add_f32_e32 v136, 1.0, v136
	v_rcp_f32_e32 v136, v136
	v_add_f32_e32 v69, 1.0, v69
	v_rcp_f32_e32 v138, v69
	v_mul_f32_e32 v69, v3, v136
	v_mul_f32_e32 v3, v51, v137
	v_mul_f32_e32 v51, v3, v138
	v_mul_f32_e32 v3, v51, v51
	v_fmac_f32_e32 v3, v69, v69
	v_mov_b32_e32 v135, v3
	s_nop 1
	v_permlane16_swap_b32_e32 v135, v3
	v_add_f32_e32 v3, v3, v135
	s_nop 1
	v_mov_b32_dpp v135, v3 row_ror:8 row_mask:0xf bank_mask:0xf
	v_add_f32_e32 v3, v3, v135
	s_nop 1
	v_mov_b32_dpp v135, v3 row_shr:4 row_mask:0xf bank_mask:0xa
	v_mov_b32_dpp v135, v3 row_shl:4 row_mask:0xf bank_mask:0x5
	v_add_f32_e32 v3, v3, v135
	s_nop 1
	v_mov_b32_dpp v135, v3 quad_perm:[2,3,0,1] row_mask:0xf bank_mask:0xf
	v_add_f32_e32 v3, v3, v135
	s_nop 1
	v_mov_b32_dpp v135, v3 quad_perm:[1,0,3,2] row_mask:0xf bank_mask:0xf
	s_and_saveexec_b64 s[6:7], vcc
	s_cbranch_execz .LBB0_833
	v_add_f32_e32 v3, v3, v135
	ds_write_b32 v83, v3 offset:4
.LBB0_833:
	s_or_b64 exec, exec, s[6:7]
	s_waitcnt vmcnt(59)
	v_lshlrev_b32_e32 v3, 16, v72
	v_mul_f32_e32 v72, 0xbfb8aa3b, v3
	s_waitcnt vmcnt(56)
	v_lshlrev_b32_e32 v70, 16, v70
	v_exp_f32_e32 v72, v72
	v_mul_f32_e32 v135, 0xbfb8aa3b, v70
	v_exp_f32_e32 v135, v135
	v_mul_f32_e32 v3, v4, v3
	v_add_f32_e32 v72, 1.0, v72
	v_rcp_f32_e32 v72, v72
	v_add_f32_e32 v135, 1.0, v135
	v_rcp_f32_e32 v135, v135
	v_mul_f32_e32 v72, v3, v72
	v_mul_f32_e32 v3, v52, v70
	v_mul_f32_e32 v70, v3, v135
	v_mul_f32_e32 v3, v70, v70
	v_fmac_f32_e32 v3, v72, v72
	v_mov_b32_e32 v4, v3
	s_nop 1
	v_permlane16_swap_b32_e32 v4, v3
	v_add_f32_e32 v3, v3, v4
	s_nop 1
	v_mov_b32_dpp v4, v3 row_ror:8 row_mask:0xf bank_mask:0xf
	v_add_f32_e32 v3, v3, v4
	s_nop 1
	v_mov_b32_dpp v4, v3 row_shr:4 row_mask:0xf bank_mask:0xa
	v_mov_b32_dpp v4, v3 row_shl:4 row_mask:0xf bank_mask:0x5
	v_add_f32_e32 v3, v3, v4
	s_nop 1
	v_mov_b32_dpp v4, v3 quad_perm:[2,3,0,1] row_mask:0xf bank_mask:0xf
	v_add_f32_e32 v3, v3, v4
	s_nop 1
	v_mov_b32_dpp v4, v3 quad_perm:[1,0,3,2] row_mask:0xf bank_mask:0xf
	s_and_saveexec_b64 s[6:7], vcc
	s_cbranch_execz .LBB0_835
	v_add_f32_e32 v3, v3, v4
	ds_write_b32 v83, v3 offset:8
.LBB0_835:
	s_or_b64 exec, exec, s[6:7]
	v_lshlrev_b32_e32 v3, 16, v73
	v_mul_f32_e32 v4, 0xbfb8aa3b, v3
	v_lshlrev_b32_e32 v52, 16, v71
	v_exp_f32_e32 v4, v4
	v_mul_f32_e32 v71, 0xbfb8aa3b, v52
	v_exp_f32_e32 v71, v71
	v_mul_f32_e32 v3, v5, v3
	v_add_f32_e32 v4, 1.0, v4
	v_rcp_f32_e32 v4, v4
	v_add_f32_e32 v71, 1.0, v71
	v_rcp_f32_e32 v71, v71
	v_mul_f32_e32 v73, v3, v4
	v_mul_f32_e32 v3, v53, v52
	v_mul_f32_e32 v71, v3, v71
	v_mul_f32_e32 v3, v71, v71
	v_fmac_f32_e32 v3, v73, v73
	v_mov_b32_e32 v4, v3
	s_nop 1
	v_permlane16_swap_b32_e32 v4, v3
	v_add_f32_e32 v3, v3, v4
	s_nop 1
	v_mov_b32_dpp v4, v3 row_ror:8 row_mask:0xf bank_mask:0xf
	v_add_f32_e32 v3, v3, v4
	s_nop 1
	v_mov_b32_dpp v4, v3 row_shr:4 row_mask:0xf bank_mask:0xa
	v_mov_b32_dpp v4, v3 row_shl:4 row_mask:0xf bank_mask:0x5
	v_add_f32_e32 v3, v3, v4
	s_nop 1
	v_mov_b32_dpp v4, v3 quad_perm:[2,3,0,1] row_mask:0xf bank_mask:0xf
	v_add_f32_e32 v3, v3, v4
	s_nop 1
	v_mov_b32_dpp v4, v3 quad_perm:[1,0,3,2] row_mask:0xf bank_mask:0xf
	s_and_saveexec_b64 s[6:7], vcc
	s_cbranch_execz .LBB0_837
	v_add_f32_e32 v3, v3, v4
	ds_write_b32 v83, v3 offset:12
.LBB0_837:
	s_or_b64 exec, exec, s[6:7]
	s_waitcnt vmcnt(55)
	v_lshlrev_b32_e32 v3, 16, v134
	v_mul_f32_e32 v4, 0xbfb8aa3b, v3
	s_waitcnt vmcnt(54)
	v_lshlrev_b32_e32 v5, 16, v133
	v_exp_f32_e32 v4, v4
	v_mul_f32_e32 v52, 0xbfb8aa3b, v5
	v_exp_f32_e32 v52, v52
	v_mul_f32_e32 v3, v6, v3
	v_add_f32_e32 v4, 1.0, v4
	v_rcp_f32_e32 v4, v4
	v_add_f32_e32 v52, 1.0, v52
	v_rcp_f32_e32 v53, v52
	v_mul_f32_e32 v52, v3, v4
	v_mul_f32_e32 v3, v54, v5
	v_mul_f32_e32 v6, v3, v53
	v_mul_f32_e32 v3, v6, v6
	v_fmac_f32_e32 v3, v52, v52
	v_mov_b32_e32 v4, v3
	s_nop 1
	v_permlane16_swap_b32_e32 v4, v3
	v_add_f32_e32 v3, v3, v4
	s_nop 1
	v_mov_b32_dpp v4, v3 row_ror:8 row_mask:0xf bank_mask:0xf
	v_add_f32_e32 v3, v3, v4
	s_nop 1
	v_mov_b32_dpp v4, v3 row_shr:4 row_mask:0xf bank_mask:0xa
	v_mov_b32_dpp v4, v3 row_shl:4 row_mask:0xf bank_mask:0x5
	v_add_f32_e32 v3, v3, v4
	s_nop 1
	v_mov_b32_dpp v4, v3 quad_perm:[2,3,0,1] row_mask:0xf bank_mask:0xf
	v_add_f32_e32 v3, v3, v4
	s_nop 1
	v_mov_b32_dpp v4, v3 quad_perm:[1,0,3,2] row_mask:0xf bank_mask:0xf
	s_and_saveexec_b64 s[6:7], vcc
	s_cbranch_execz .LBB0_839
	v_add_f32_e32 v3, v3, v4
	ds_write_b32 v83, v3 offset:32
.LBB0_839:
	s_or_b64 exec, exec, s[6:7]
	s_waitcnt vmcnt(53)
	v_lshlrev_b32_e32 v3, 16, v132
	v_mul_f32_e32 v4, 0xbfb8aa3b, v3
	s_waitcnt vmcnt(52)
	v_lshlrev_b32_e32 v5, 16, v131
	v_exp_f32_e32 v4, v4
	v_mul_f32_e32 v53, 0xbfb8aa3b, v5
	v_exp_f32_e32 v53, v53
	v_mul_f32_e32 v3, v7, v3
	v_add_f32_e32 v4, 1.0, v4
	v_rcp_f32_e32 v4, v4
	v_add_f32_e32 v53, 1.0, v53
	v_rcp_f32_e32 v54, v53
	v_mul_f32_e32 v53, v3, v4
	v_mul_f32_e32 v3, v55, v5
	v_mul_f32_e32 v7, v3, v54
	v_mul_f32_e32 v3, v7, v7
	v_fmac_f32_e32 v3, v53, v53
	v_mov_b32_e32 v4, v3
	s_nop 1
	v_permlane16_swap_b32_e32 v4, v3
	v_add_f32_e32 v3, v3, v4
	s_nop 1
	v_mov_b32_dpp v4, v3 row_ror:8 row_mask:0xf bank_mask:0xf
	v_add_f32_e32 v3, v3, v4
	s_nop 1
	v_mov_b32_dpp v4, v3 row_shr:4 row_mask:0xf bank_mask:0xa
	v_mov_b32_dpp v4, v3 row_shl:4 row_mask:0xf bank_mask:0x5
	v_add_f32_e32 v3, v3, v4
	s_nop 1
	v_mov_b32_dpp v4, v3 quad_perm:[2,3,0,1] row_mask:0xf bank_mask:0xf
	v_add_f32_e32 v3, v3, v4
	s_nop 1
	v_mov_b32_dpp v4, v3 quad_perm:[1,0,3,2] row_mask:0xf bank_mask:0xf
	s_and_saveexec_b64 s[6:7], vcc
	s_cbranch_execz .LBB0_841
	v_add_f32_e32 v3, v3, v4
	ds_write_b32 v83, v3 offset:36
.LBB0_841:
	s_or_b64 exec, exec, s[6:7]
	s_waitcnt vmcnt(51)
	v_lshlrev_b32_e32 v3, 16, v130
	v_mul_f32_e32 v4, 0xbfb8aa3b, v3
	s_waitcnt vmcnt(50)
	v_lshlrev_b32_e32 v5, 16, v129
	v_exp_f32_e32 v4, v4
	v_mul_f32_e32 v54, 0xbfb8aa3b, v5
	v_exp_f32_e32 v54, v54
	v_mul_f32_e32 v3, v8, v3
	v_add_f32_e32 v4, 1.0, v4
	v_rcp_f32_e32 v4, v4
	v_add_f32_e32 v54, 1.0, v54
	v_rcp_f32_e32 v54, v54
	v_mul_f32_e32 v55, v3, v4
	v_mul_f32_e32 v3, v56, v5
	v_mul_f32_e32 v54, v3, v54
	v_mul_f32_e32 v3, v54, v54
	v_fmac_f32_e32 v3, v55, v55
	v_mov_b32_e32 v4, v3
	s_nop 1
	v_permlane16_swap_b32_e32 v4, v3
	v_add_f32_e32 v3, v3, v4
	s_nop 1
	v_mov_b32_dpp v4, v3 row_ror:8 row_mask:0xf bank_mask:0xf
	v_add_f32_e32 v3, v3, v4
	s_nop 1
	v_mov_b32_dpp v4, v3 row_shr:4 row_mask:0xf bank_mask:0xa
	v_mov_b32_dpp v4, v3 row_shl:4 row_mask:0xf bank_mask:0x5
	v_add_f32_e32 v3, v3, v4
	s_nop 1
	v_mov_b32_dpp v4, v3 quad_perm:[2,3,0,1] row_mask:0xf bank_mask:0xf
	v_add_f32_e32 v3, v3, v4
	s_nop 1
	v_mov_b32_dpp v4, v3 quad_perm:[1,0,3,2] row_mask:0xf bank_mask:0xf
	s_and_saveexec_b64 s[6:7], vcc
	s_cbranch_execz .LBB0_843
	v_add_f32_e32 v3, v3, v4
	ds_write_b32 v83, v3 offset:40
.LBB0_843:
	s_or_b64 exec, exec, s[6:7]
	s_waitcnt vmcnt(49)
	v_lshlrev_b32_e32 v3, 16, v128
	v_mul_f32_e32 v4, 0xbfb8aa3b, v3
	s_waitcnt vmcnt(48)
	v_lshlrev_b32_e32 v5, 16, v74
	v_exp_f32_e32 v4, v4
	v_mul_f32_e32 v8, 0xbfb8aa3b, v5
	v_exp_f32_e32 v8, v8
	v_mul_f32_e32 v3, v9, v3
	v_add_f32_e32 v4, 1.0, v4
	v_rcp_f32_e32 v4, v4
	v_add_f32_e32 v8, 1.0, v8
	v_rcp_f32_e32 v8, v8
	v_mul_f32_e32 v74, v3, v4
	v_mul_f32_e32 v3, v57, v5
	v_mul_f32_e32 v57, v3, v8
	v_mul_f32_e32 v3, v57, v57
	v_fmac_f32_e32 v3, v74, v74
	v_mov_b32_e32 v4, v3
	s_nop 1
	v_permlane16_swap_b32_e32 v4, v3
	v_add_f32_e32 v3, v3, v4
	s_nop 1
	v_mov_b32_dpp v4, v3 row_ror:8 row_mask:0xf bank_mask:0xf
	v_add_f32_e32 v3, v3, v4
	s_nop 1
	v_mov_b32_dpp v4, v3 row_shr:4 row_mask:0xf bank_mask:0xa
	v_mov_b32_dpp v4, v3 row_shl:4 row_mask:0xf bank_mask:0x5
	v_add_f32_e32 v3, v3, v4
	s_nop 1
	v_mov_b32_dpp v4, v3 quad_perm:[2,3,0,1] row_mask:0xf bank_mask:0xf
	v_add_f32_e32 v3, v3, v4
	s_nop 1
	v_mov_b32_dpp v4, v3 quad_perm:[1,0,3,2] row_mask:0xf bank_mask:0xf
	s_and_saveexec_b64 s[6:7], vcc
	s_cbranch_execz .LBB0_845
	v_add_f32_e32 v3, v3, v4
	ds_write_b32 v83, v3 offset:44
.LBB0_845:
	s_or_b64 exec, exec, s[6:7]
	s_waitcnt vmcnt(47)
	v_lshlrev_b32_e32 v3, 16, v127
	v_mul_f32_e32 v4, 0xbfb8aa3b, v3
	s_waitcnt vmcnt(46)
	v_lshlrev_b32_e32 v5, 16, v126
	v_exp_f32_e32 v4, v4
	v_mul_f32_e32 v8, 0xbfb8aa3b, v5
	v_exp_f32_e32 v8, v8
	v_mul_f32_e32 v3, v10, v3
	v_add_f32_e32 v4, 1.0, v4
	v_rcp_f32_e32 v4, v4
	v_add_f32_e32 v8, 1.0, v8
	v_rcp_f32_e32 v8, v8
	v_mul_f32_e32 v9, v3, v4
	v_mul_f32_e32 v3, v58, v5
	v_mul_f32_e32 v8, v3, v8
	v_mul_f32_e32 v3, v8, v8
	v_fmac_f32_e32 v3, v9, v9
	v_mov_b32_e32 v4, v3
	s_nop 1
	v_permlane16_swap_b32_e32 v4, v3
	v_add_f32_e32 v3, v3, v4
	s_nop 1
	v_mov_b32_dpp v4, v3 row_ror:8 row_mask:0xf bank_mask:0xf
	v_add_f32_e32 v3, v3, v4
	s_nop 1
	v_mov_b32_dpp v4, v3 row_shr:4 row_mask:0xf bank_mask:0xa
	v_mov_b32_dpp v4, v3 row_shl:4 row_mask:0xf bank_mask:0x5
	v_add_f32_e32 v3, v3, v4
	s_nop 1
	v_mov_b32_dpp v4, v3 quad_perm:[2,3,0,1] row_mask:0xf bank_mask:0xf
	v_add_f32_e32 v3, v3, v4
	s_nop 1
	v_mov_b32_dpp v4, v3 quad_perm:[1,0,3,2] row_mask:0xf bank_mask:0xf
	s_and_saveexec_b64 s[6:7], vcc
	s_cbranch_execz .LBB0_847
	v_add_f32_e32 v3, v3, v4
	ds_write_b32 v83, v3 offset:64
.LBB0_847:
	s_or_b64 exec, exec, s[6:7]
	s_waitcnt vmcnt(45)
	v_lshlrev_b32_e32 v3, 16, v125
	v_mul_f32_e32 v4, 0xbfb8aa3b, v3
	s_waitcnt vmcnt(44)
	v_lshlrev_b32_e32 v5, 16, v124
	v_exp_f32_e32 v4, v4
	v_mul_f32_e32 v10, 0xbfb8aa3b, v5
	v_exp_f32_e32 v10, v10
	v_mul_f32_e32 v3, v11, v3
	v_add_f32_e32 v4, 1.0, v4
	v_rcp_f32_e32 v4, v4
	v_add_f32_e32 v10, 1.0, v10
	v_rcp_f32_e32 v10, v10
	v_mul_f32_e32 v56, v3, v4
	v_mul_f32_e32 v3, v59, v5
	v_mul_f32_e32 v10, v3, v10
	v_mul_f32_e32 v3, v10, v10
	v_fmac_f32_e32 v3, v56, v56
	v_mov_b32_e32 v4, v3
	s_nop 1
	v_permlane16_swap_b32_e32 v4, v3
	v_add_f32_e32 v3, v3, v4
	s_nop 1
	v_mov_b32_dpp v4, v3 row_ror:8 row_mask:0xf bank_mask:0xf
	v_add_f32_e32 v3, v3, v4
	s_nop 1
	v_mov_b32_dpp v4, v3 row_shr:4 row_mask:0xf bank_mask:0xa
	v_mov_b32_dpp v4, v3 row_shl:4 row_mask:0xf bank_mask:0x5
	v_add_f32_e32 v3, v3, v4
	s_nop 1
	v_mov_b32_dpp v4, v3 quad_perm:[2,3,0,1] row_mask:0xf bank_mask:0xf
	v_add_f32_e32 v3, v3, v4
	s_nop 1
	v_mov_b32_dpp v4, v3 quad_perm:[1,0,3,2] row_mask:0xf bank_mask:0xf
	s_and_saveexec_b64 s[6:7], vcc
	s_cbranch_execz .LBB0_849
	v_add_f32_e32 v3, v3, v4
	ds_write_b32 v83, v3 offset:68
.LBB0_849:
	s_or_b64 exec, exec, s[6:7]
	s_waitcnt vmcnt(43)
	v_lshlrev_b32_e32 v3, 16, v123
	v_mul_f32_e32 v4, 0xbfb8aa3b, v3
	s_waitcnt vmcnt(42)
	v_lshlrev_b32_e32 v5, 16, v122
	v_exp_f32_e32 v4, v4
	v_mul_f32_e32 v11, 0xbfb8aa3b, v5
	v_exp_f32_e32 v11, v11
	v_mul_f32_e32 v3, v12, v3
	v_add_f32_e32 v4, 1.0, v4
	v_rcp_f32_e32 v4, v4
	v_add_f32_e32 v11, 1.0, v11
	v_rcp_f32_e32 v11, v11
	v_mul_f32_e32 v59, v3, v4
	v_mul_f32_e32 v3, v60, v5
	v_mul_f32_e32 v58, v3, v11
	v_mul_f32_e32 v3, v58, v58
	v_fmac_f32_e32 v3, v59, v59
	v_mov_b32_e32 v4, v3
	s_nop 1
	v_permlane16_swap_b32_e32 v4, v3
	v_add_f32_e32 v3, v3, v4
	s_nop 1
	v_mov_b32_dpp v4, v3 row_ror:8 row_mask:0xf bank_mask:0xf
	v_add_f32_e32 v3, v3, v4
	s_nop 1
	v_mov_b32_dpp v4, v3 row_shr:4 row_mask:0xf bank_mask:0xa
	v_mov_b32_dpp v4, v3 row_shl:4 row_mask:0xf bank_mask:0x5
	v_add_f32_e32 v3, v3, v4
	s_nop 1
	v_mov_b32_dpp v4, v3 quad_perm:[2,3,0,1] row_mask:0xf bank_mask:0xf
	v_add_f32_e32 v3, v3, v4
	s_nop 1
	v_mov_b32_dpp v4, v3 quad_perm:[1,0,3,2] row_mask:0xf bank_mask:0xf
	s_and_saveexec_b64 s[6:7], vcc
	s_cbranch_execz .LBB0_851
	v_add_f32_e32 v3, v3, v4
	ds_write_b32 v83, v3 offset:72
.LBB0_851:
	s_or_b64 exec, exec, s[6:7]
	s_waitcnt vmcnt(41)
	v_lshlrev_b32_e32 v3, 16, v121
	v_mul_f32_e32 v4, 0xbfb8aa3b, v3
	s_waitcnt vmcnt(40)
	v_lshlrev_b32_e32 v5, 16, v75
	v_exp_f32_e32 v4, v4
	v_mul_f32_e32 v11, 0xbfb8aa3b, v5
	v_exp_f32_e32 v11, v11
	v_mul_f32_e32 v3, v13, v3
	v_add_f32_e32 v4, 1.0, v4
	v_rcp_f32_e32 v4, v4
	v_add_f32_e32 v11, 1.0, v11
	v_rcp_f32_e32 v11, v11
	v_mul_f32_e32 v75, v3, v4
	v_mul_f32_e32 v3, v61, v5
	v_mul_f32_e32 v61, v3, v11
	v_mul_f32_e32 v3, v61, v61
	v_fmac_f32_e32 v3, v75, v75
	v_mov_b32_e32 v4, v3
	s_nop 1
	v_permlane16_swap_b32_e32 v4, v3
	v_add_f32_e32 v3, v3, v4
	s_nop 1
	v_mov_b32_dpp v4, v3 row_ror:8 row_mask:0xf bank_mask:0xf
	v_add_f32_e32 v3, v3, v4
	s_nop 1
	v_mov_b32_dpp v4, v3 row_shr:4 row_mask:0xf bank_mask:0xa
	v_mov_b32_dpp v4, v3 row_shl:4 row_mask:0xf bank_mask:0x5
	v_add_f32_e32 v3, v3, v4
	s_nop 1
	v_mov_b32_dpp v4, v3 quad_perm:[2,3,0,1] row_mask:0xf bank_mask:0xf
	v_add_f32_e32 v3, v3, v4
	s_nop 1
	v_mov_b32_dpp v4, v3 quad_perm:[1,0,3,2] row_mask:0xf bank_mask:0xf
	s_and_saveexec_b64 s[6:7], vcc
	s_cbranch_execz .LBB0_853
	v_add_f32_e32 v3, v3, v4
	ds_write_b32 v83, v3 offset:76
.LBB0_853:
	s_or_b64 exec, exec, s[6:7]
	s_waitcnt vmcnt(39)
	v_lshlrev_b32_e32 v3, 16, v120
	v_mul_f32_e32 v4, 0xbfb8aa3b, v3
	s_waitcnt vmcnt(38)
	v_lshlrev_b32_e32 v5, 16, v119
	v_exp_f32_e32 v4, v4
	v_mul_f32_e32 v11, 0xbfb8aa3b, v5
	v_exp_f32_e32 v11, v11
	v_mul_f32_e32 v3, v14, v3
	v_add_f32_e32 v4, 1.0, v4
	v_rcp_f32_e32 v4, v4
	v_add_f32_e32 v11, 1.0, v11
	v_rcp_f32_e32 v11, v11
	v_mul_f32_e32 v12, v3, v4
	v_mul_f32_e32 v3, v62, v5
	v_mul_f32_e32 v11, v3, v11
	v_mul_f32_e32 v3, v11, v11
	v_fmac_f32_e32 v3, v12, v12
	v_mov_b32_e32 v4, v3
	s_nop 1
	v_permlane16_swap_b32_e32 v4, v3
	v_add_f32_e32 v3, v3, v4
	s_nop 1
	v_mov_b32_dpp v4, v3 row_ror:8 row_mask:0xf bank_mask:0xf
	v_add_f32_e32 v3, v3, v4
	s_nop 1
	v_mov_b32_dpp v4, v3 row_shr:4 row_mask:0xf bank_mask:0xa
	v_mov_b32_dpp v4, v3 row_shl:4 row_mask:0xf bank_mask:0x5
	v_add_f32_e32 v3, v3, v4
	s_nop 1
	v_mov_b32_dpp v4, v3 quad_perm:[2,3,0,1] row_mask:0xf bank_mask:0xf
	v_add_f32_e32 v3, v3, v4
	s_nop 1
	v_mov_b32_dpp v4, v3 quad_perm:[1,0,3,2] row_mask:0xf bank_mask:0xf
	s_and_saveexec_b64 s[6:7], vcc
	s_cbranch_execz .LBB0_855
	v_add_f32_e32 v3, v3, v4
	ds_write_b32 v83, v3 offset:96
.LBB0_855:
	s_or_b64 exec, exec, s[6:7]
	s_waitcnt vmcnt(37)
	v_lshlrev_b32_e32 v3, 16, v118
	v_mul_f32_e32 v4, 0xbfb8aa3b, v3
	s_waitcnt vmcnt(36)
	v_lshlrev_b32_e32 v5, 16, v117
	v_exp_f32_e32 v4, v4
	v_mul_f32_e32 v13, 0xbfb8aa3b, v5
	v_exp_f32_e32 v13, v13
	v_mul_f32_e32 v3, v15, v3
	v_add_f32_e32 v4, 1.0, v4
	v_rcp_f32_e32 v4, v4
	v_add_f32_e32 v13, 1.0, v13
	v_rcp_f32_e32 v13, v13
	v_mul_f32_e32 v60, v3, v4
	v_mul_f32_e32 v3, v63, v5
	v_mul_f32_e32 v13, v3, v13
	v_mul_f32_e32 v3, v13, v13
	v_fmac_f32_e32 v3, v60, v60
	v_mov_b32_e32 v4, v3
	s_nop 1
	v_permlane16_swap_b32_e32 v4, v3
	v_add_f32_e32 v3, v3, v4
	s_nop 1
	v_mov_b32_dpp v4, v3 row_ror:8 row_mask:0xf bank_mask:0xf
	v_add_f32_e32 v3, v3, v4
	s_nop 1
	v_mov_b32_dpp v4, v3 row_shr:4 row_mask:0xf bank_mask:0xa
	v_mov_b32_dpp v4, v3 row_shl:4 row_mask:0xf bank_mask:0x5
	v_add_f32_e32 v3, v3, v4
	s_nop 1
	v_mov_b32_dpp v4, v3 quad_perm:[2,3,0,1] row_mask:0xf bank_mask:0xf
	v_add_f32_e32 v3, v3, v4
	s_nop 1
	v_mov_b32_dpp v4, v3 quad_perm:[1,0,3,2] row_mask:0xf bank_mask:0xf
	s_and_saveexec_b64 s[6:7], vcc
	s_cbranch_execz .LBB0_857
	v_add_f32_e32 v3, v3, v4
	ds_write_b32 v83, v3 offset:100
.LBB0_857:
	s_or_b64 exec, exec, s[6:7]
	s_waitcnt vmcnt(35)
	v_lshlrev_b32_e32 v3, 16, v116
	v_mul_f32_e32 v4, 0xbfb8aa3b, v3
	s_waitcnt vmcnt(34)
	v_lshlrev_b32_e32 v5, 16, v115
	v_exp_f32_e32 v4, v4
	v_mul_f32_e32 v14, 0xbfb8aa3b, v5
	v_exp_f32_e32 v14, v14
	v_mul_f32_e32 v3, v16, v3
	v_add_f32_e32 v4, 1.0, v4
	v_rcp_f32_e32 v4, v4
	v_add_f32_e32 v14, 1.0, v14
	v_rcp_f32_e32 v14, v14
	v_mul_f32_e32 v62, v3, v4
	v_mul_f32_e32 v3, v64, v5
	v_mul_f32_e32 v16, v3, v14
	v_mul_f32_e32 v3, v16, v16
	v_fmac_f32_e32 v3, v62, v62
	v_mov_b32_e32 v4, v3
	s_nop 1
	v_permlane16_swap_b32_e32 v4, v3
	v_add_f32_e32 v3, v3, v4
	s_nop 1
	v_mov_b32_dpp v4, v3 row_ror:8 row_mask:0xf bank_mask:0xf
	v_add_f32_e32 v3, v3, v4
	s_nop 1
	v_mov_b32_dpp v4, v3 row_shr:4 row_mask:0xf bank_mask:0xa
	v_mov_b32_dpp v4, v3 row_shl:4 row_mask:0xf bank_mask:0x5
	v_add_f32_e32 v3, v3, v4
	s_nop 1
	v_mov_b32_dpp v4, v3 quad_perm:[2,3,0,1] row_mask:0xf bank_mask:0xf
	v_add_f32_e32 v3, v3, v4
	s_nop 1
	v_mov_b32_dpp v4, v3 quad_perm:[1,0,3,2] row_mask:0xf bank_mask:0xf
	s_and_saveexec_b64 s[6:7], vcc
	s_cbranch_execz .LBB0_859
	v_add_f32_e32 v3, v3, v4
	ds_write_b32 v83, v3 offset:104
.LBB0_859:
	s_or_b64 exec, exec, s[6:7]
	s_waitcnt vmcnt(33)
	v_lshlrev_b32_e32 v3, 16, v114
	v_mul_f32_e32 v4, 0xbfb8aa3b, v3
	s_waitcnt vmcnt(32)
	v_lshlrev_b32_e32 v5, 16, v113
	v_exp_f32_e32 v4, v4
	v_mul_f32_e32 v14, 0xbfb8aa3b, v5
	v_exp_f32_e32 v14, v14
	v_mul_f32_e32 v3, v17, v3
	v_add_f32_e32 v4, 1.0, v4
	v_rcp_f32_e32 v4, v4
	v_add_f32_e32 v14, 1.0, v14
	v_rcp_f32_e32 v14, v14
	v_mul_f32_e32 v64, v3, v4
	v_mul_f32_e32 v3, v65, v5
	v_mul_f32_e32 v63, v3, v14
	v_mul_f32_e32 v3, v63, v63
	v_fmac_f32_e32 v3, v64, v64
	v_mov_b32_e32 v4, v3
	s_nop 1
	v_permlane16_swap_b32_e32 v4, v3
	v_add_f32_e32 v3, v3, v4
	s_nop 1
	v_mov_b32_dpp v4, v3 row_ror:8 row_mask:0xf bank_mask:0xf
	v_add_f32_e32 v3, v3, v4
	s_nop 1
	v_mov_b32_dpp v4, v3 row_shr:4 row_mask:0xf bank_mask:0xa
	v_mov_b32_dpp v4, v3 row_shl:4 row_mask:0xf bank_mask:0x5
	v_add_f32_e32 v3, v3, v4
	s_nop 1
	v_mov_b32_dpp v4, v3 quad_perm:[2,3,0,1] row_mask:0xf bank_mask:0xf
	v_add_f32_e32 v3, v3, v4
	s_nop 1
	v_mov_b32_dpp v4, v3 quad_perm:[1,0,3,2] row_mask:0xf bank_mask:0xf
	s_and_saveexec_b64 s[6:7], vcc
	s_cbranch_execz .LBB0_861
	v_add_f32_e32 v3, v3, v4
	ds_write_b32 v83, v3 offset:108
.LBB0_861:
	s_or_b64 exec, exec, s[6:7]
	s_waitcnt vmcnt(31)
	v_lshlrev_b32_e32 v3, 16, v112
	v_mul_f32_e32 v4, 0xbfb8aa3b, v3
	s_waitcnt vmcnt(30)
	v_lshlrev_b32_e32 v5, 16, v111
	v_exp_f32_e32 v4, v4
	v_mul_f32_e32 v14, 0xbfb8aa3b, v5
	v_exp_f32_e32 v14, v14
	v_mul_f32_e32 v3, v18, v3
	v_add_f32_e32 v4, 1.0, v4
	v_rcp_f32_e32 v4, v4
	v_add_f32_e32 v14, 1.0, v14
	v_rcp_f32_e32 v14, v14
	v_mul_f32_e32 v15, v3, v4
	v_mul_f32_e32 v3, v34, v5
	v_mul_f32_e32 v14, v3, v14
	v_mul_f32_e32 v3, v14, v14
	v_fmac_f32_e32 v3, v15, v15
	v_mov_b32_e32 v4, v3
	s_nop 1
	v_permlane16_swap_b32_e32 v4, v3
	v_add_f32_e32 v3, v3, v4
	s_nop 1
	v_mov_b32_dpp v4, v3 row_ror:8 row_mask:0xf bank_mask:0xf
	v_add_f32_e32 v3, v3, v4
	s_nop 1
	v_mov_b32_dpp v4, v3 row_shr:4 row_mask:0xf bank_mask:0xa
	v_mov_b32_dpp v4, v3 row_shl:4 row_mask:0xf bank_mask:0x5
	v_add_f32_e32 v3, v3, v4
	s_nop 1
	v_mov_b32_dpp v4, v3 quad_perm:[2,3,0,1] row_mask:0xf bank_mask:0xf
	v_add_f32_e32 v3, v3, v4
	s_nop 1
	v_mov_b32_dpp v4, v3 quad_perm:[1,0,3,2] row_mask:0xf bank_mask:0xf
	s_and_saveexec_b64 s[6:7], vcc
	s_cbranch_execz .LBB0_863
	v_add_f32_e32 v3, v3, v4
	ds_write_b32 v83, v3 offset:128
.LBB0_863:
	s_or_b64 exec, exec, s[6:7]
	s_waitcnt vmcnt(29)
	v_lshlrev_b32_e32 v3, 16, v110
	v_mul_f32_e32 v4, 0xbfb8aa3b, v3
	s_waitcnt vmcnt(28)
	v_lshlrev_b32_e32 v5, 16, v109
	v_exp_f32_e32 v4, v4
	v_mul_f32_e32 v17, 0xbfb8aa3b, v5
	v_exp_f32_e32 v17, v17
	v_mul_f32_e32 v3, v19, v3
	v_add_f32_e32 v4, 1.0, v4
	v_rcp_f32_e32 v4, v4
	v_add_f32_e32 v17, 1.0, v17
	v_rcp_f32_e32 v17, v17
	v_mul_f32_e32 v34, v3, v4
	v_mul_f32_e32 v3, v35, v5
	v_mul_f32_e32 v17, v3, v17
	v_mul_f32_e32 v3, v17, v17
	v_fmac_f32_e32 v3, v34, v34
	v_mov_b32_e32 v4, v3
	s_nop 1
	v_permlane16_swap_b32_e32 v4, v3
	v_add_f32_e32 v3, v3, v4
	s_nop 1
	v_mov_b32_dpp v4, v3 row_ror:8 row_mask:0xf bank_mask:0xf
	v_add_f32_e32 v3, v3, v4
	s_nop 1
	v_mov_b32_dpp v4, v3 row_shr:4 row_mask:0xf bank_mask:0xa
	v_mov_b32_dpp v4, v3 row_shl:4 row_mask:0xf bank_mask:0x5
	v_add_f32_e32 v3, v3, v4
	s_nop 1
	v_mov_b32_dpp v4, v3 quad_perm:[2,3,0,1] row_mask:0xf bank_mask:0xf
	v_add_f32_e32 v3, v3, v4
	s_nop 1
	v_mov_b32_dpp v4, v3 quad_perm:[1,0,3,2] row_mask:0xf bank_mask:0xf
	s_and_saveexec_b64 s[6:7], vcc
	s_cbranch_execz .LBB0_865
	v_add_f32_e32 v3, v3, v4
	ds_write_b32 v83, v3 offset:132
.LBB0_865:
	s_or_b64 exec, exec, s[6:7]
	s_waitcnt vmcnt(27)
	v_lshlrev_b32_e32 v3, 16, v108
	v_mul_f32_e32 v4, 0xbfb8aa3b, v3
	s_waitcnt vmcnt(26)
	v_lshlrev_b32_e32 v5, 16, v107
	v_exp_f32_e32 v4, v4
	v_mul_f32_e32 v18, 0xbfb8aa3b, v5
	v_exp_f32_e32 v18, v18
	v_mul_f32_e32 v3, v20, v3
	v_add_f32_e32 v4, 1.0, v4
	v_rcp_f32_e32 v4, v4
	v_add_f32_e32 v18, 1.0, v18
	v_rcp_f32_e32 v18, v18
	v_mul_f32_e32 v35, v3, v4
	v_mul_f32_e32 v3, v36, v5
	v_mul_f32_e32 v20, v3, v18
	v_mul_f32_e32 v3, v20, v20
	v_fmac_f32_e32 v3, v35, v35
	v_mov_b32_e32 v4, v3
	s_nop 1
	v_permlane16_swap_b32_e32 v4, v3
	v_add_f32_e32 v3, v3, v4
	s_nop 1
	v_mov_b32_dpp v4, v3 row_ror:8 row_mask:0xf bank_mask:0xf
	v_add_f32_e32 v3, v3, v4
	s_nop 1
	v_mov_b32_dpp v4, v3 row_shr:4 row_mask:0xf bank_mask:0xa
	v_mov_b32_dpp v4, v3 row_shl:4 row_mask:0xf bank_mask:0x5
	v_add_f32_e32 v3, v3, v4
	s_nop 1
	v_mov_b32_dpp v4, v3 quad_perm:[2,3,0,1] row_mask:0xf bank_mask:0xf
	v_add_f32_e32 v3, v3, v4
	s_nop 1
	v_mov_b32_dpp v4, v3 quad_perm:[1,0,3,2] row_mask:0xf bank_mask:0xf
	s_and_saveexec_b64 s[6:7], vcc
	s_cbranch_execz .LBB0_867
	v_add_f32_e32 v3, v3, v4
	ds_write_b32 v83, v3 offset:136
.LBB0_867:
	s_or_b64 exec, exec, s[6:7]
	s_waitcnt vmcnt(25)
	v_lshlrev_b32_e32 v3, 16, v106
	v_mul_f32_e32 v4, 0xbfb8aa3b, v3
	s_waitcnt vmcnt(24)
	v_lshlrev_b32_e32 v5, 16, v105
	v_exp_f32_e32 v4, v4
	v_mul_f32_e32 v18, 0xbfb8aa3b, v5
	v_exp_f32_e32 v18, v18
	v_mul_f32_e32 v3, v21, v3
	v_add_f32_e32 v4, 1.0, v4
	v_rcp_f32_e32 v4, v4
	v_add_f32_e32 v18, 1.0, v18
	v_rcp_f32_e32 v18, v18
	v_mul_f32_e32 v65, v3, v4
	v_mul_f32_e32 v3, v37, v5
	v_mul_f32_e32 v37, v3, v18
	v_mul_f32_e32 v3, v37, v37
	v_fmac_f32_e32 v3, v65, v65
	v_mov_b32_e32 v4, v3
	s_nop 1
	v_permlane16_swap_b32_e32 v4, v3
	v_add_f32_e32 v3, v3, v4
	s_nop 1
	v_mov_b32_dpp v4, v3 row_ror:8 row_mask:0xf bank_mask:0xf
	v_add_f32_e32 v3, v3, v4
	s_nop 1
	v_mov_b32_dpp v4, v3 row_shr:4 row_mask:0xf bank_mask:0xa
	v_mov_b32_dpp v4, v3 row_shl:4 row_mask:0xf bank_mask:0x5
	v_add_f32_e32 v3, v3, v4
	s_nop 1
	v_mov_b32_dpp v4, v3 quad_perm:[2,3,0,1] row_mask:0xf bank_mask:0xf
	v_add_f32_e32 v3, v3, v4
	s_nop 1
	v_mov_b32_dpp v4, v3 quad_perm:[1,0,3,2] row_mask:0xf bank_mask:0xf
	s_and_saveexec_b64 s[6:7], vcc
	s_cbranch_execz .LBB0_869
	v_add_f32_e32 v3, v3, v4
	ds_write_b32 v83, v3 offset:140
.LBB0_869:
	s_or_b64 exec, exec, s[6:7]
	s_waitcnt vmcnt(23)
	v_lshlrev_b32_e32 v3, 16, v104
	v_mul_f32_e32 v4, 0xbfb8aa3b, v3
	s_waitcnt vmcnt(22)
	v_lshlrev_b32_e32 v5, 16, v103
	v_exp_f32_e32 v4, v4
	v_mul_f32_e32 v18, 0xbfb8aa3b, v5
	v_exp_f32_e32 v18, v18
	v_mul_f32_e32 v3, v22, v3
	v_add_f32_e32 v4, 1.0, v4
	v_rcp_f32_e32 v4, v4
	v_add_f32_e32 v18, 1.0, v18
	v_rcp_f32_e32 v18, v18
	v_mul_f32_e32 v19, v3, v4
	v_mul_f32_e32 v3, v38, v5
	v_mul_f32_e32 v18, v3, v18
	v_mul_f32_e32 v3, v18, v18
	v_fmac_f32_e32 v3, v19, v19
	v_mov_b32_e32 v4, v3
	s_nop 1
	v_permlane16_swap_b32_e32 v4, v3
	v_add_f32_e32 v3, v3, v4
	s_nop 1
	v_mov_b32_dpp v4, v3 row_ror:8 row_mask:0xf bank_mask:0xf
	v_add_f32_e32 v3, v3, v4
	s_nop 1
	v_mov_b32_dpp v4, v3 row_shr:4 row_mask:0xf bank_mask:0xa
	v_mov_b32_dpp v4, v3 row_shl:4 row_mask:0xf bank_mask:0x5
	v_add_f32_e32 v3, v3, v4
	s_nop 1
	v_mov_b32_dpp v4, v3 quad_perm:[2,3,0,1] row_mask:0xf bank_mask:0xf
	v_add_f32_e32 v3, v3, v4
	s_nop 1
	v_mov_b32_dpp v4, v3 quad_perm:[1,0,3,2] row_mask:0xf bank_mask:0xf
	s_and_saveexec_b64 s[6:7], vcc
	s_cbranch_execz .LBB0_871
	v_add_f32_e32 v3, v3, v4
	ds_write_b32 v83, v3 offset:160
.LBB0_871:
	s_or_b64 exec, exec, s[6:7]
	s_waitcnt vmcnt(21)
	v_lshlrev_b32_e32 v3, 16, v102
	v_mul_f32_e32 v4, 0xbfb8aa3b, v3
	s_waitcnt vmcnt(20)
	v_lshlrev_b32_e32 v5, 16, v101
	v_exp_f32_e32 v4, v4
	v_mul_f32_e32 v21, 0xbfb8aa3b, v5
	v_exp_f32_e32 v21, v21
	v_mul_f32_e32 v3, v23, v3
	v_add_f32_e32 v4, 1.0, v4
	v_rcp_f32_e32 v4, v4
	v_add_f32_e32 v21, 1.0, v21
	v_rcp_f32_e32 v21, v21
	v_mul_f32_e32 v36, v3, v4
	v_mul_f32_e32 v3, v39, v5
	v_mul_f32_e32 v21, v3, v21
	v_mul_f32_e32 v3, v21, v21
	v_fmac_f32_e32 v3, v36, v36
	v_mov_b32_e32 v4, v3
	s_nop 1
	v_permlane16_swap_b32_e32 v4, v3
	v_add_f32_e32 v3, v3, v4
	s_nop 1
	v_mov_b32_dpp v4, v3 row_ror:8 row_mask:0xf bank_mask:0xf
	v_add_f32_e32 v3, v3, v4
	s_nop 1
	v_mov_b32_dpp v4, v3 row_shr:4 row_mask:0xf bank_mask:0xa
	v_mov_b32_dpp v4, v3 row_shl:4 row_mask:0xf bank_mask:0x5
	v_add_f32_e32 v3, v3, v4
	s_nop 1
	v_mov_b32_dpp v4, v3 quad_perm:[2,3,0,1] row_mask:0xf bank_mask:0xf
	v_add_f32_e32 v3, v3, v4
	s_nop 1
	v_mov_b32_dpp v4, v3 quad_perm:[1,0,3,2] row_mask:0xf bank_mask:0xf
	s_and_saveexec_b64 s[6:7], vcc
	s_cbranch_execz .LBB0_873
	v_add_f32_e32 v3, v3, v4
	ds_write_b32 v83, v3 offset:164
.LBB0_873:
	s_or_b64 exec, exec, s[6:7]
	s_waitcnt vmcnt(19)
	v_lshlrev_b32_e32 v3, 16, v100
	v_mul_f32_e32 v4, 0xbfb8aa3b, v3
	s_waitcnt vmcnt(18)
	v_lshlrev_b32_e32 v5, 16, v99
	v_exp_f32_e32 v4, v4
	v_mul_f32_e32 v22, 0xbfb8aa3b, v5
	v_exp_f32_e32 v22, v22
	v_mul_f32_e32 v3, v24, v3
	v_add_f32_e32 v4, 1.0, v4
	v_rcp_f32_e32 v4, v4
	v_add_f32_e32 v22, 1.0, v22
	v_rcp_f32_e32 v22, v22
	v_mul_f32_e32 v38, v3, v4
	v_mul_f32_e32 v3, v40, v5
	v_mul_f32_e32 v24, v3, v22
	v_mul_f32_e32 v3, v24, v24
	v_fmac_f32_e32 v3, v38, v38
	v_mov_b32_e32 v4, v3
	s_nop 1
	v_permlane16_swap_b32_e32 v4, v3
	v_add_f32_e32 v3, v3, v4
	s_nop 1
	v_mov_b32_dpp v4, v3 row_ror:8 row_mask:0xf bank_mask:0xf
	v_add_f32_e32 v3, v3, v4
	s_nop 1
	v_mov_b32_dpp v4, v3 row_shr:4 row_mask:0xf bank_mask:0xa
	v_mov_b32_dpp v4, v3 row_shl:4 row_mask:0xf bank_mask:0x5
	v_add_f32_e32 v3, v3, v4
	s_nop 1
	v_mov_b32_dpp v4, v3 quad_perm:[2,3,0,1] row_mask:0xf bank_mask:0xf
	v_add_f32_e32 v3, v3, v4
	s_nop 1
	v_mov_b32_dpp v4, v3 quad_perm:[1,0,3,2] row_mask:0xf bank_mask:0xf
	s_and_saveexec_b64 s[6:7], vcc
	s_cbranch_execz .LBB0_875
	v_add_f32_e32 v3, v3, v4
	ds_write_b32 v83, v3 offset:168
.LBB0_875:
	s_or_b64 exec, exec, s[6:7]
	s_waitcnt vmcnt(17)
	v_lshlrev_b32_e32 v3, 16, v98
	v_mul_f32_e32 v4, 0xbfb8aa3b, v3
	s_waitcnt vmcnt(16)
	v_lshlrev_b32_e32 v5, 16, v85
	v_exp_f32_e32 v4, v4
	v_mul_f32_e32 v22, 0xbfb8aa3b, v5
	v_exp_f32_e32 v22, v22
	v_mul_f32_e32 v3, v25, v3
	v_add_f32_e32 v4, 1.0, v4
	v_rcp_f32_e32 v4, v4
	v_add_f32_e32 v22, 1.0, v22
	v_rcp_f32_e32 v22, v22
	v_mul_f32_e32 v85, v3, v4
	v_mul_f32_e32 v3, v41, v5
	v_mul_f32_e32 v40, v3, v22
	v_mul_f32_e32 v3, v40, v40
	v_fmac_f32_e32 v3, v85, v85
	v_mov_b32_e32 v4, v3
	s_nop 1
	v_permlane16_swap_b32_e32 v4, v3
	v_add_f32_e32 v3, v3, v4
	s_nop 1
	v_mov_b32_dpp v4, v3 row_ror:8 row_mask:0xf bank_mask:0xf
	v_add_f32_e32 v3, v3, v4
	s_nop 1
	v_mov_b32_dpp v4, v3 row_shr:4 row_mask:0xf bank_mask:0xa
	v_mov_b32_dpp v4, v3 row_shl:4 row_mask:0xf bank_mask:0x5
	v_add_f32_e32 v3, v3, v4
	s_nop 1
	v_mov_b32_dpp v4, v3 quad_perm:[2,3,0,1] row_mask:0xf bank_mask:0xf
	v_add_f32_e32 v3, v3, v4
	s_nop 1
	v_mov_b32_dpp v4, v3 quad_perm:[1,0,3,2] row_mask:0xf bank_mask:0xf
	s_and_saveexec_b64 s[6:7], vcc
	s_cbranch_execz .LBB0_877
	v_add_f32_e32 v3, v3, v4
	ds_write_b32 v83, v3 offset:172
.LBB0_877:
	s_or_b64 exec, exec, s[6:7]
	s_waitcnt vmcnt(15)
	v_lshlrev_b32_e32 v3, 16, v97
	v_mul_f32_e32 v4, 0xbfb8aa3b, v3
	s_waitcnt vmcnt(14)
	v_lshlrev_b32_e32 v5, 16, v96
	v_exp_f32_e32 v4, v4
	v_mul_f32_e32 v22, 0xbfb8aa3b, v5
	v_exp_f32_e32 v22, v22
	v_mul_f32_e32 v3, v26, v3
	v_add_f32_e32 v4, 1.0, v4
	v_rcp_f32_e32 v4, v4
	v_add_f32_e32 v22, 1.0, v22
	v_rcp_f32_e32 v22, v22
	v_mul_f32_e32 v23, v3, v4
	v_mul_f32_e32 v3, v42, v5
	v_mul_f32_e32 v22, v3, v22
	v_mul_f32_e32 v3, v22, v22
	v_fmac_f32_e32 v3, v23, v23
	v_mov_b32_e32 v4, v3
	s_nop 1
	v_permlane16_swap_b32_e32 v4, v3
	v_add_f32_e32 v3, v3, v4
	s_nop 1
	v_mov_b32_dpp v4, v3 row_ror:8 row_mask:0xf bank_mask:0xf
	v_add_f32_e32 v3, v3, v4
	s_nop 1
	v_mov_b32_dpp v4, v3 row_shr:4 row_mask:0xf bank_mask:0xa
	v_mov_b32_dpp v4, v3 row_shl:4 row_mask:0xf bank_mask:0x5
	v_add_f32_e32 v3, v3, v4
	s_nop 1
	v_mov_b32_dpp v4, v3 quad_perm:[2,3,0,1] row_mask:0xf bank_mask:0xf
	v_add_f32_e32 v3, v3, v4
	s_nop 1
	v_mov_b32_dpp v4, v3 quad_perm:[1,0,3,2] row_mask:0xf bank_mask:0xf
	s_and_saveexec_b64 s[6:7], vcc
	s_cbranch_execz .LBB0_879
	v_add_f32_e32 v3, v3, v4
	ds_write_b32 v83, v3 offset:192
.LBB0_879:
	s_or_b64 exec, exec, s[6:7]
	s_waitcnt vmcnt(13)
	v_lshlrev_b32_e32 v3, 16, v95
	v_mul_f32_e32 v4, 0xbfb8aa3b, v3
	s_waitcnt vmcnt(12)
	v_lshlrev_b32_e32 v5, 16, v94
	v_exp_f32_e32 v4, v4
	v_mul_f32_e32 v25, 0xbfb8aa3b, v5
	v_exp_f32_e32 v25, v25
	v_mul_f32_e32 v3, v27, v3
	v_add_f32_e32 v4, 1.0, v4
	v_rcp_f32_e32 v4, v4
	v_add_f32_e32 v25, 1.0, v25
	v_rcp_f32_e32 v25, v25
	v_mul_f32_e32 v39, v3, v4
	v_mul_f32_e32 v3, v43, v5
	v_mul_f32_e32 v25, v3, v25
	v_mul_f32_e32 v3, v25, v25
	v_fmac_f32_e32 v3, v39, v39
	v_mov_b32_e32 v4, v3
	s_nop 1
	v_permlane16_swap_b32_e32 v4, v3
	v_add_f32_e32 v3, v3, v4
	s_nop 1
	v_mov_b32_dpp v4, v3 row_ror:8 row_mask:0xf bank_mask:0xf
	v_add_f32_e32 v3, v3, v4
	s_nop 1
	v_mov_b32_dpp v4, v3 row_shr:4 row_mask:0xf bank_mask:0xa
	v_mov_b32_dpp v4, v3 row_shl:4 row_mask:0xf bank_mask:0x5
	v_add_f32_e32 v3, v3, v4
	s_nop 1
	v_mov_b32_dpp v4, v3 quad_perm:[2,3,0,1] row_mask:0xf bank_mask:0xf
	v_add_f32_e32 v3, v3, v4
	s_nop 1
	v_mov_b32_dpp v4, v3 quad_perm:[1,0,3,2] row_mask:0xf bank_mask:0xf
	s_and_saveexec_b64 s[6:7], vcc
	s_cbranch_execz .LBB0_881
	v_add_f32_e32 v3, v3, v4
	ds_write_b32 v83, v3 offset:196
.LBB0_881:
	s_or_b64 exec, exec, s[6:7]
	s_waitcnt vmcnt(11)
	v_lshlrev_b32_e32 v3, 16, v93
	v_mul_f32_e32 v4, 0xbfb8aa3b, v3
	s_waitcnt vmcnt(10)
	v_lshlrev_b32_e32 v5, 16, v92
	v_exp_f32_e32 v4, v4
	v_mul_f32_e32 v26, 0xbfb8aa3b, v5
	v_exp_f32_e32 v26, v26
	v_mul_f32_e32 v3, v28, v3
	v_add_f32_e32 v4, 1.0, v4
	v_rcp_f32_e32 v4, v4
	v_add_f32_e32 v26, 1.0, v26
	v_rcp_f32_e32 v26, v26
	v_mul_f32_e32 v41, v3, v4
	v_mul_f32_e32 v3, v44, v5
	v_mul_f32_e32 v28, v3, v26
	v_mul_f32_e32 v3, v28, v28
	v_fmac_f32_e32 v3, v41, v41
	v_mov_b32_e32 v4, v3
	s_nop 1
	v_permlane16_swap_b32_e32 v4, v3
	v_add_f32_e32 v3, v3, v4
	s_nop 1
	v_mov_b32_dpp v4, v3 row_ror:8 row_mask:0xf bank_mask:0xf
	v_add_f32_e32 v3, v3, v4
	s_nop 1
	v_mov_b32_dpp v4, v3 row_shr:4 row_mask:0xf bank_mask:0xa
	v_mov_b32_dpp v4, v3 row_shl:4 row_mask:0xf bank_mask:0x5
	v_add_f32_e32 v3, v3, v4
	s_nop 1
	v_mov_b32_dpp v4, v3 quad_perm:[2,3,0,1] row_mask:0xf bank_mask:0xf
	v_add_f32_e32 v3, v3, v4
	s_nop 1
	v_mov_b32_dpp v4, v3 quad_perm:[1,0,3,2] row_mask:0xf bank_mask:0xf
	s_and_saveexec_b64 s[6:7], vcc
	s_cbranch_execz .LBB0_883
	v_add_f32_e32 v3, v3, v4
	ds_write_b32 v83, v3 offset:200
.LBB0_883:
	s_or_b64 exec, exec, s[6:7]
	s_waitcnt vmcnt(9)
	v_lshlrev_b32_e32 v3, 16, v91
	v_mul_f32_e32 v4, 0xbfb8aa3b, v3
	s_waitcnt vmcnt(8)
	v_lshlrev_b32_e32 v5, 16, v90
	v_exp_f32_e32 v4, v4
	v_mul_f32_e32 v26, 0xbfb8aa3b, v5
	v_exp_f32_e32 v26, v26
	v_mul_f32_e32 v3, v29, v3
	v_add_f32_e32 v4, 1.0, v4
	v_rcp_f32_e32 v4, v4
	v_add_f32_e32 v26, 1.0, v26
	v_rcp_f32_e32 v26, v26
	v_mul_f32_e32 v43, v3, v4
	v_mul_f32_e32 v3, v45, v5
	v_mul_f32_e32 v42, v3, v26
	v_mul_f32_e32 v3, v42, v42
	v_fmac_f32_e32 v3, v43, v43
	v_mov_b32_e32 v4, v3
	s_nop 1
	v_permlane16_swap_b32_e32 v4, v3
	v_add_f32_e32 v3, v3, v4
	s_nop 1
	v_mov_b32_dpp v4, v3 row_ror:8 row_mask:0xf bank_mask:0xf
	v_add_f32_e32 v3, v3, v4
	s_nop 1
	v_mov_b32_dpp v4, v3 row_shr:4 row_mask:0xf bank_mask:0xa
	v_mov_b32_dpp v4, v3 row_shl:4 row_mask:0xf bank_mask:0x5
	v_add_f32_e32 v3, v3, v4
	s_nop 1
	v_mov_b32_dpp v4, v3 quad_perm:[2,3,0,1] row_mask:0xf bank_mask:0xf
	v_add_f32_e32 v3, v3, v4
	s_nop 1
	v_mov_b32_dpp v4, v3 quad_perm:[1,0,3,2] row_mask:0xf bank_mask:0xf
	s_and_saveexec_b64 s[6:7], vcc
	s_cbranch_execz .LBB0_885
	v_add_f32_e32 v3, v3, v4
	ds_write_b32 v83, v3 offset:204
.LBB0_885:
	s_or_b64 exec, exec, s[6:7]
	s_waitcnt vmcnt(7)
	v_lshlrev_b32_e32 v3, 16, v89
	v_mul_f32_e32 v4, 0xbfb8aa3b, v3
	s_waitcnt vmcnt(6)
	v_lshlrev_b32_e32 v5, 16, v88
	v_exp_f32_e32 v4, v4
	v_mul_f32_e32 v26, 0xbfb8aa3b, v5
	v_exp_f32_e32 v26, v26
	v_mul_f32_e32 v3, v30, v3
	v_add_f32_e32 v4, 1.0, v4
	v_rcp_f32_e32 v4, v4
	v_add_f32_e32 v26, 1.0, v26
	v_rcp_f32_e32 v26, v26
	v_mul_f32_e32 v27, v3, v4
	v_mul_f32_e32 v3, v46, v5
	v_mul_f32_e32 v26, v3, v26
	v_mul_f32_e32 v3, v26, v26
	v_fmac_f32_e32 v3, v27, v27
	v_mov_b32_e32 v4, v3
	s_nop 1
	v_permlane16_swap_b32_e32 v4, v3
	v_add_f32_e32 v3, v3, v4
	s_nop 1
	v_mov_b32_dpp v4, v3 row_ror:8 row_mask:0xf bank_mask:0xf
	v_add_f32_e32 v3, v3, v4
	s_nop 1
	v_mov_b32_dpp v4, v3 row_shr:4 row_mask:0xf bank_mask:0xa
	v_mov_b32_dpp v4, v3 row_shl:4 row_mask:0xf bank_mask:0x5
	v_add_f32_e32 v3, v3, v4
	s_nop 1
	v_mov_b32_dpp v4, v3 quad_perm:[2,3,0,1] row_mask:0xf bank_mask:0xf
	v_add_f32_e32 v3, v3, v4
	s_nop 1
	v_mov_b32_dpp v4, v3 quad_perm:[1,0,3,2] row_mask:0xf bank_mask:0xf
	s_and_saveexec_b64 s[6:7], vcc
	s_cbranch_execz .LBB0_887
	v_add_f32_e32 v3, v3, v4
	ds_write_b32 v83, v3 offset:224
.LBB0_887:
	s_or_b64 exec, exec, s[6:7]
	s_waitcnt vmcnt(5)
	v_lshlrev_b32_e32 v3, 16, v87
	v_mul_f32_e32 v4, 0xbfb8aa3b, v3
	s_waitcnt vmcnt(4)
	v_lshlrev_b32_e32 v5, 16, v86
	v_exp_f32_e32 v4, v4
	v_mul_f32_e32 v29, 0xbfb8aa3b, v5
	v_exp_f32_e32 v29, v29
	v_mul_f32_e32 v3, v31, v3
	v_add_f32_e32 v4, 1.0, v4
	v_rcp_f32_e32 v4, v4
	v_add_f32_e32 v29, 1.0, v29
	v_rcp_f32_e32 v29, v29
	v_mul_f32_e32 v30, v3, v4
	v_mul_f32_e32 v3, v47, v5
	v_mul_f32_e32 v29, v3, v29
	v_mul_f32_e32 v3, v29, v29
	v_fmac_f32_e32 v3, v30, v30
	v_mov_b32_e32 v4, v3
	s_nop 1
	v_permlane16_swap_b32_e32 v4, v3
	v_add_f32_e32 v3, v3, v4
	s_nop 1
	v_mov_b32_dpp v4, v3 row_ror:8 row_mask:0xf bank_mask:0xf
	v_add_f32_e32 v3, v3, v4
	s_nop 1
	v_mov_b32_dpp v4, v3 row_shr:4 row_mask:0xf bank_mask:0xa
	v_mov_b32_dpp v4, v3 row_shl:4 row_mask:0xf bank_mask:0x5
	v_add_f32_e32 v3, v3, v4
	s_nop 1
	v_mov_b32_dpp v4, v3 quad_perm:[2,3,0,1] row_mask:0xf bank_mask:0xf
	v_add_f32_e32 v3, v3, v4
	s_nop 1
	v_mov_b32_dpp v4, v3 quad_perm:[1,0,3,2] row_mask:0xf bank_mask:0xf
	s_and_saveexec_b64 s[6:7], vcc
	s_cbranch_execz .LBB0_889
	v_add_f32_e32 v3, v3, v4
	ds_write_b32 v83, v3 offset:228
.LBB0_889:
	s_or_b64 exec, exec, s[6:7]
	s_waitcnt vmcnt(3)
	v_lshlrev_b32_e32 v3, 16, v82
	v_mul_f32_e32 v4, 0xbfb8aa3b, v3
	s_waitcnt vmcnt(2)
	v_lshlrev_b32_e32 v5, 16, v79
	v_exp_f32_e32 v4, v4
	v_mul_f32_e32 v31, 0xbfb8aa3b, v5
	v_exp_f32_e32 v31, v31
	v_mul_f32_e32 v3, v32, v3
	v_add_f32_e32 v4, 1.0, v4
	v_rcp_f32_e32 v4, v4
	v_add_f32_e32 v31, 1.0, v31
	v_rcp_f32_e32 v31, v31
	v_mul_f32_e32 v32, v3, v4
	v_mul_f32_e32 v3, v48, v5
	v_mul_f32_e32 v31, v3, v31
	v_mul_f32_e32 v3, v31, v31
	v_fmac_f32_e32 v3, v32, v32
	v_mov_b32_e32 v4, v3
	s_nop 1
	v_permlane16_swap_b32_e32 v4, v3
	v_add_f32_e32 v3, v3, v4
	s_nop 1
	v_mov_b32_dpp v4, v3 row_ror:8 row_mask:0xf bank_mask:0xf
	v_add_f32_e32 v3, v3, v4
	s_nop 1
	v_mov_b32_dpp v4, v3 row_shr:4 row_mask:0xf bank_mask:0xa
	v_mov_b32_dpp v4, v3 row_shl:4 row_mask:0xf bank_mask:0x5
	v_add_f32_e32 v3, v3, v4
	s_nop 1
	v_mov_b32_dpp v4, v3 quad_perm:[2,3,0,1] row_mask:0xf bank_mask:0xf
	v_add_f32_e32 v3, v3, v4
	s_nop 1
	v_mov_b32_dpp v4, v3 quad_perm:[1,0,3,2] row_mask:0xf bank_mask:0xf
	s_and_saveexec_b64 s[6:7], vcc
	s_cbranch_execz .LBB0_891
	v_add_f32_e32 v3, v3, v4
	ds_write_b32 v83, v3 offset:232
.LBB0_891:
	s_or_b64 exec, exec, s[6:7]
	s_waitcnt vmcnt(1)
	v_lshlrev_b32_e32 v3, 16, v77
	v_mul_f32_e32 v4, 0xbfb8aa3b, v3
	s_waitcnt vmcnt(0)
	v_lshlrev_b32_e32 v5, 16, v76
	v_exp_f32_e32 v4, v4
	v_mul_f32_e32 v44, 0xbfb8aa3b, v5
	v_exp_f32_e32 v44, v44
	v_mul_f32_e32 v3, v33, v3
	v_add_f32_e32 v4, 1.0, v4
	v_rcp_f32_e32 v4, v4
	v_add_f32_e32 v44, 1.0, v44
	v_rcp_f32_e32 v45, v44
	v_mul_f32_e32 v44, v3, v4
	v_mul_f32_e32 v3, v49, v5
	v_mul_f32_e32 v33, v3, v45
	v_mul_f32_e32 v3, v33, v33
	v_fmac_f32_e32 v3, v44, v44
	v_mov_b32_e32 v4, v3
	s_nop 1
	v_permlane16_swap_b32_e32 v4, v3
	v_add_f32_e32 v3, v3, v4
	s_nop 1
	v_mov_b32_dpp v2, v3 row_ror:8 row_mask:0xf bank_mask:0xf
	v_add_f32_e32 v2, v3, v2
	s_nop 1
	v_mov_b32_dpp v3, v2 row_shr:4 row_mask:0xf bank_mask:0xa
	v_mov_b32_dpp v3, v2 row_shl:4 row_mask:0xf bank_mask:0x5
	v_add_f32_e32 v2, v2, v3
	s_nop 1
	v_mov_b32_dpp v3, v2 quad_perm:[2,3,0,1] row_mask:0xf bank_mask:0xf
	v_add_f32_e32 v2, v2, v3
	s_nop 1
	v_mov_b32_dpp v3, v2 quad_perm:[1,0,3,2] row_mask:0xf bank_mask:0xf
	s_and_saveexec_b64 s[6:7], vcc
	s_cbranch_execz .LBB0_623
	v_add_f32_e32 v2, v2, v3
	ds_write_b32 v83, v2 offset:236
	s_branch .LBB0_623
